# v18 + grid barrier: non-leader workgroups poll the top-level generation word directly (one round trip less per barrier)
# baseline (speedup 1.0000x reference)
.LBB0_112:
	s_lshl_b32 s0, s36, 8
	s_add_u32 s23, s34, s0
	s_addc_u32 s22, s35, 0
	v_mov_b32_e32 v1, s23
	v_add_co_u32_e32 v4, vcc, 0x1000, v1
	v_mov_b32_e32 v1, s22
	s_nop 0
	v_addc_co_u32_e32 v5, vcc, 0, v1, vcc
	v_mov_b32_e32 v1, 1
	flat_atomic_add v1, v[4:5], v1 offset:1024 sc0
	v_cvt_f32_u32_e32 v3, v2
	v_sub_u32_e32 v4, 0, v2
	v_rcp_iflag_f32_e32 v3, v3
	s_nop 0
	v_mul_f32_e32 v3, 0x4f7ffffe, v3
	v_cvt_u32_f32_e32 v3, v3
	v_mul_lo_u32 v4, v4, v3
	v_mul_hi_u32 v4, v3, v4
	v_add_u32_e32 v3, v3, v4
	s_waitcnt vmcnt(0) lgkmcnt(0)
	v_mul_hi_u32 v3, v1, v3
	v_mul_lo_u32 v5, v3, v2
	v_add_u32_e32 v4, 1, v1
	v_sub_u32_e32 v1, v1, v5
	v_add_u32_e32 v6, 1, v3
	v_cmp_ge_u32_e32 vcc, v1, v2
	v_sub_u32_e32 v5, v1, v2
	s_nop 0
	v_cndmask_b32_e32 v3, v3, v6, vcc
	v_cndmask_b32_e32 v1, v1, v5, vcc
	v_add_u32_e32 v5, 1, v3
	v_cmp_ge_u32_e32 vcc, v1, v2
	s_nop 1
	v_cndmask_b32_e32 v1, v3, v5, vcc
	v_mad_u64_u32 v[2:3], s[0:1], v2, v1, v[2:3]
	v_cmp_ne_u32_e32 vcc, v4, v2
	s_and_saveexec_b64 s[0:1], vcc
	s_xor_b64 s[0:1], exec, s[0:1]
	s_cbranch_execz .LBB0_125
	v_mov_b32_e32 v0, s34
	v_add_co_u32_e32 v2, vcc, 0x3100, v0
	v_mov_b32_e32 v0, s35
	s_nop 0
	v_addc_co_u32_e32 v3, vcc, 0, v0, vcc
	flat_load_dword v0, v[2:3] offset:1024 sc1
	s_add_u32 s6, s34, 0x3500
	s_addc_u32 s7, s35, 0
	s_waitcnt vmcnt(0) lgkmcnt(0)
	v_cmp_eq_u32_e32 vcc, v0, v1
	s_and_saveexec_b64 s[4:5], vcc
	s_cbranch_execz .LBB0_124
	s_mov_b32 s24, 1
	s_mov_b64 s[8:9], 0
	s_branch .LBB0_116

.LBB0_265:
	v_readlane_b32 s4, v254, 37
	s_lshl_b32 s4, s4, 2
	s_add_u32 s25, s2, s4
	s_addc_u32 s24, s3, 0
	v_mov_b32_e32 v1, s25
	v_add_co_u32_e32 v4, vcc, 0x1000, v1
	v_mov_b32_e32 v1, s24
	s_nop 0
	v_addc_co_u32_e32 v5, vcc, 0, v1, vcc
	flat_atomic_add v3, v[4:5], v193 offset:1024 sc0
	v_cvt_f32_u32_e32 v1, v2
	v_sub_u32_e32 v4, 0, v2
	v_rcp_iflag_f32_e32 v1, v1
	s_nop 0
	v_mul_f32_e32 v1, 0x4f7ffffe, v1
	v_cvt_u32_f32_e32 v1, v1
	v_mul_lo_u32 v4, v4, v1
	v_mul_hi_u32 v4, v1, v4
	v_add_u32_e32 v1, v1, v4
	s_waitcnt vmcnt(0) lgkmcnt(0)
	v_mul_hi_u32 v1, v3, v1
	v_mul_lo_u32 v4, v1, v2
	v_sub_u32_e32 v4, v3, v4
	v_cmp_ge_u32_e32 vcc, v4, v2
	v_add_u32_e32 v5, 1, v1
	s_nop 0
	v_cndmask_b32_e32 v1, v1, v5, vcc
	v_sub_u32_e32 v5, v4, v2
	v_cndmask_b32_e32 v4, v4, v5, vcc
	v_cmp_ge_u32_e32 vcc, v4, v2
	v_add_u32_e32 v4, 1, v1
	s_nop 0
	v_cndmask_b32_e32 v1, v1, v4, vcc
	v_add_u32_e32 v4, 1, v3
	v_mad_u64_u32 v[2:3], s[4:5], v2, v1, v[2:3]
	v_cmp_ne_u32_e32 vcc, v4, v2
	s_and_saveexec_b64 s[4:5], vcc
	s_xor_b64 s[4:5], exec, s[4:5]
	s_cbranch_execz .LBB0_278
	v_mov_b32_e32 v0, s2
	v_add_co_u32_e32 v2, vcc, 0x3100, v0
	v_mov_b32_e32 v0, s3
	s_nop 0
	v_addc_co_u32_e32 v3, vcc, 0, v0, vcc
	flat_load_dword v0, v[2:3] offset:1024 sc1
	s_add_u32 s8, s2, 0x3500
	s_addc_u32 s9, s3, 0
	s_waitcnt vmcnt(0) lgkmcnt(0)
	v_cmp_eq_u32_e32 vcc, v0, v1
	s_and_saveexec_b64 s[6:7], vcc
	s_cbranch_execz .LBB0_277
	s_mov_b32 s26, 1
	s_mov_b64 s[10:11], 0
	s_branch .LBB0_269

.LBB0_353:
	v_readlane_b32 s4, v254, 37
	s_lshl_b32 s4, s4, 2
	s_add_u32 s27, s2, s4
	s_addc_u32 s26, s3, 0
	v_mov_b32_e32 v1, s27
	v_add_co_u32_e32 v4, vcc, 0x1000, v1
	v_mov_b32_e32 v1, s26
	s_nop 0
	v_addc_co_u32_e32 v5, vcc, 0, v1, vcc
	flat_atomic_add v3, v[4:5], v193 offset:1024 sc0
	v_cvt_f32_u32_e32 v1, v2
	v_sub_u32_e32 v4, 0, v2
	v_rcp_iflag_f32_e32 v1, v1
	s_nop 0
	v_mul_f32_e32 v1, 0x4f7ffffe, v1
	v_cvt_u32_f32_e32 v1, v1
	v_mul_lo_u32 v4, v4, v1
	v_mul_hi_u32 v4, v1, v4
	v_add_u32_e32 v1, v1, v4
	s_waitcnt vmcnt(0) lgkmcnt(0)
	v_mul_hi_u32 v1, v3, v1
	v_mul_lo_u32 v4, v1, v2
	v_sub_u32_e32 v4, v3, v4
	v_cmp_ge_u32_e32 vcc, v4, v2
	v_add_u32_e32 v5, 1, v1
	s_nop 0
	v_cndmask_b32_e32 v1, v1, v5, vcc
	v_sub_u32_e32 v5, v4, v2
	v_cndmask_b32_e32 v4, v4, v5, vcc
	v_cmp_ge_u32_e32 vcc, v4, v2
	v_add_u32_e32 v4, 1, v1
	s_nop 0
	v_cndmask_b32_e32 v1, v1, v4, vcc
	v_add_u32_e32 v4, 1, v3
	v_mad_u64_u32 v[2:3], s[4:5], v2, v1, v[2:3]
	v_cmp_ne_u32_e32 vcc, v4, v2
	s_and_saveexec_b64 s[4:5], vcc
	s_xor_b64 s[4:5], exec, s[4:5]
	s_cbranch_execz .LBB0_366
	v_mov_b32_e32 v0, s2
	v_add_co_u32_e32 v2, vcc, 0x3100, v0
	v_mov_b32_e32 v0, s3
	s_nop 0
	v_addc_co_u32_e32 v3, vcc, 0, v0, vcc
	flat_load_dword v0, v[2:3] offset:1024 sc1
	s_add_u32 s8, s2, 0x3500
	s_addc_u32 s9, s3, 0
	s_waitcnt vmcnt(0) lgkmcnt(0)
	v_cmp_eq_u32_e32 vcc, v0, v1
	s_and_saveexec_b64 s[6:7], vcc
	s_cbranch_execz .LBB0_365
	s_mov_b32 s30, 1
	s_mov_b64 s[12:13], 0
	s_branch .LBB0_357

.LBB0_583:
	v_readlane_b32 s6, v254, 37
	s_lshl_b32 s6, s6, 2
	s_add_u32 s30, s2, s6
	s_addc_u32 s29, s3, 0
	v_mov_b32_e32 v1, s30
	v_add_co_u32_e32 v4, vcc, 0x1000, v1
	v_mov_b32_e32 v1, s29
	s_nop 0
	v_addc_co_u32_e32 v5, vcc, 0, v1, vcc
	flat_atomic_add v3, v[4:5], v193 offset:1024 sc0
	v_cvt_f32_u32_e32 v1, v2
	v_sub_u32_e32 v4, 0, v2
	v_rcp_iflag_f32_e32 v1, v1
	s_nop 0
	v_mul_f32_e32 v1, 0x4f7ffffe, v1
	v_cvt_u32_f32_e32 v1, v1
	v_mul_lo_u32 v4, v4, v1
	v_mul_hi_u32 v4, v1, v4
	v_add_u32_e32 v1, v1, v4
	s_waitcnt vmcnt(0) lgkmcnt(0)
	v_mul_hi_u32 v1, v3, v1
	v_mul_lo_u32 v4, v1, v2
	v_sub_u32_e32 v4, v3, v4
	v_cmp_ge_u32_e32 vcc, v4, v2
	v_add_u32_e32 v5, 1, v1
	s_nop 0
	v_cndmask_b32_e32 v1, v1, v5, vcc
	v_sub_u32_e32 v5, v4, v2
	v_cndmask_b32_e32 v4, v4, v5, vcc
	v_cmp_ge_u32_e32 vcc, v4, v2
	v_add_u32_e32 v4, 1, v1
	s_nop 0
	v_cndmask_b32_e32 v1, v1, v4, vcc
	v_add_u32_e32 v4, 1, v3
	v_mad_u64_u32 v[2:3], s[6:7], v2, v1, v[2:3]
	v_cmp_ne_u32_e32 vcc, v4, v2
	s_and_saveexec_b64 s[6:7], vcc
	s_xor_b64 s[6:7], exec, s[6:7]
	s_cbranch_execz .LBB0_596
	v_mov_b32_e32 v0, s2
	v_add_co_u32_e32 v2, vcc, 0x3100, v0
	v_mov_b32_e32 v0, s3
	s_nop 0
	v_addc_co_u32_e32 v3, vcc, 0, v0, vcc
	flat_load_dword v0, v[2:3] offset:1024 sc1
	s_add_u32 s12, s2, 0x3500
	s_addc_u32 s13, s3, 0
	s_waitcnt vmcnt(0) lgkmcnt(0)
	v_cmp_eq_u32_e32 vcc, v0, v1
	s_and_saveexec_b64 s[8:9], vcc
	s_cbranch_execz .LBB0_595
	s_mov_b32 s33, 1
	s_mov_b64 s[14:15], 0
	s_branch .LBB0_587

.LBB0_689:
	v_readlane_b32 s4, v254, 37
	s_lshl_b32 s4, s4, 2
	s_add_u32 s9, s2, s4
	s_addc_u32 s8, s3, 0
	v_mov_b32_e32 v1, s9
	v_add_co_u32_e32 v4, vcc, 0x1000, v1
	v_mov_b32_e32 v1, s8
	s_nop 0
	v_addc_co_u32_e32 v5, vcc, 0, v1, vcc
	flat_atomic_add v3, v[4:5], v193 offset:1024 sc0
	v_cvt_f32_u32_e32 v1, v2
	v_sub_u32_e32 v4, 0, v2
	v_rcp_iflag_f32_e32 v1, v1
	s_nop 0
	v_mul_f32_e32 v1, 0x4f7ffffe, v1
	v_cvt_u32_f32_e32 v1, v1
	v_mul_lo_u32 v4, v4, v1
	v_mul_hi_u32 v4, v1, v4
	v_add_u32_e32 v1, v1, v4
	s_waitcnt vmcnt(0) lgkmcnt(0)
	v_mul_hi_u32 v1, v3, v1
	v_mul_lo_u32 v4, v1, v2
	v_sub_u32_e32 v4, v3, v4
	v_cmp_ge_u32_e32 vcc, v4, v2
	v_add_u32_e32 v5, 1, v1
	s_nop 0
	v_cndmask_b32_e32 v1, v1, v5, vcc
	v_sub_u32_e32 v5, v4, v2
	v_cndmask_b32_e32 v4, v4, v5, vcc
	v_cmp_ge_u32_e32 vcc, v4, v2
	v_add_u32_e32 v4, 1, v1
	s_nop 0
	v_cndmask_b32_e32 v1, v1, v4, vcc
	v_add_u32_e32 v4, 1, v3
	v_mad_u64_u32 v[2:3], s[4:5], v2, v1, v[2:3]
	v_cmp_ne_u32_e32 vcc, v4, v2
	s_and_saveexec_b64 s[4:5], vcc
	s_xor_b64 s[4:5], exec, s[4:5]
	s_cbranch_execz .LBB0_702
	v_mov_b32_e32 v0, s2
	v_add_co_u32_e32 v2, vcc, 0x3100, v0
	v_mov_b32_e32 v0, s3
	s_nop 0
	v_addc_co_u32_e32 v3, vcc, 0, v0, vcc
	flat_load_dword v0, v[2:3] offset:1024 sc1
	s_add_u32 s10, s2, 0x3500
	s_addc_u32 s11, s3, 0
	s_waitcnt vmcnt(0) lgkmcnt(0)
	v_cmp_eq_u32_e32 vcc, v0, v1
	s_and_saveexec_b64 s[6:7], vcc
	s_cbranch_execz .LBB0_701
	s_mov_b32 s26, 1
	s_mov_b64 s[12:13], 0
	s_branch .LBB0_693
